# strategy 4: static s_setprio 1 for waves 8-15 of both layer kernels
# baseline (speedup 1.0000x reference)
.LBB4_14:
	v_lshrrev_b32_e32 v2, 3, v0
	s_load_dwordx2 s[4:5], s[0:1], 0x40
	v_and_b32_e32 v2, 0x78, v2
	s_movk_i32 s2, 0xa0
	v_and_b32_e32 v97, 7, v0
	s_sub_i32 s0, s18, s8
	v_and_b32_e32 v1, 63, v0
	v_mov_b32_e32 v89, 0
	v_mad_u32_u24 v3, v2, s2, 0
	v_bfe_u32 v96, v0, 3, 3
	v_and_b32_e32 v99, 15, v0
	v_bfe_u32 v4, v0, 4, 2
	s_add_i32 s0, s0, 7
	v_mul_u32_u24_e32 v5, 0xa0, v97
	v_and_b32_e32 v0, 48, v0
	s_ashr_i32 s9, s0, 3
	v_cmp_eq_u32_e64 s[0:1], 0, v1
	v_mad_u32_u24 v1, v96, s2, v3
	v_lshlrev_b32_e32 v2, 3, v4
	v_add3_u32 v103, v3, v5, v0
	v_mov_b32_e32 v3, v89
	v_lshlrev_b32_e32 v98, 4, v97
	v_add_u32_e32 v0, 0, v0
	v_lshlrev_b32_e32 v88, 2, v4
	v_lshl_add_u64 v[90:91], s[22:23], 0, v[2:3]
	v_mul_u32_u24_e32 v2, 0x220, v99
	v_or_b32_e32 v100, 8, v97
	v_or_b32_e32 v101, 16, v97
	v_add_u32_e32 v102, 0, v98
	v_cmp_gt_u32_e64 s[2:3], 8, v99
	s_waitcnt lgkmcnt(0)
	v_lshl_add_u64 v[92:93], s[4:5], 0, v[88:89]
	v_lshlrev_b32_e32 v88, 2, v88
	v_add_u32_e32 v104, v1, v98
	v_add_u32_e32 v105, v0, v2
	v_add_u32_e32 v105, 0x1cd90, v105
	s_lshl_b32 s19, s36, 3
	s_add_i32 s19, s19, s8
	v_add_u32_e32 v94, s19, v96
	v_cmp_gt_i32_e64 s[4:5], s18, v94
	v_mov_b32_e32 v32, 0
	v_mov_b32_e32 v33, 0
	v_mov_b32_e32 v34, 0
	v_mov_b32_e32 v35, 0
	s_and_saveexec_b64 s[6:7], s[4:5]
	v_lshl_add_u32 v36, v94, 1, v94
	v_lshlrev_b32_e32 v36, 2, v36
	global_load_dwordx4 v[32:35], v36, s[10:11]
	s_mov_b64 exec, s[6:7]
	s_waitcnt vmcnt(6)
	ds_write_b128 v40, v[6:9]
	s_waitcnt vmcnt(5)
	ds_write_b128 v40, v[10:13] offset:17408
	s_waitcnt vmcnt(4)
	ds_write_b128 v41, v[14:17]
	s_waitcnt vmcnt(3)
	ds_write_b128 v41, v[18:21] offset:16384
	s_waitcnt vmcnt(2)
	ds_write_b128 v41, v[22:25] offset:32768
	s_waitcnt vmcnt(1)
	ds_write_b128 v41, v[26:29] offset:49152
	s_and_saveexec_b64 s[6:7], s[34:35]
	ds_write_b128 v38, v[42:45]
	s_mov_b64 exec, s[6:7]
	s_waitcnt vmcnt(0)
	v_sub_u32_e32 v72, v33, v32
	v_sub_u32_e32 v108, v34, v33
	v_sub_u32_e32 v35, v35, v34
	v_add_lshl_u32 v37, v32, v97, 2
	v_add_lshl_u32 v38, v33, v97, 2
	v_add_lshl_u32 v39, v34, v97, 2
	v_mov_b32_e32 v36, 0x4000000
	v_mov_b32_e32 v68, 0x4000000
	v_mov_b32_e32 v74, 0x4000000
	v_mov_b32_e32 v85, 0x4000000
	v_mov_b32_e32 v84, 0x4000000
	v_mov_b32_e32 v109, 0x4000000
	v_mov_b32_e32 v107, 0x4000000
	v_mov_b32_e32 v106, 0x4000000
	v_mov_b32_e32 v95, 0x4000000
	s_mov_b64 s[6:7], exec
	v_cmp_lt_i32_e32 vcc, v97, v72
	s_and_b64 exec, exec, vcc
	global_load_dword v36, v37, s[12:13]
	v_cmp_lt_i32_e32 vcc, v100, v72
	s_and_b64 exec, exec, vcc
	global_load_dword v68, v37, s[12:13] offset:32
	v_cmp_lt_i32_e32 vcc, v101, v72
	s_and_b64 exec, exec, vcc
	global_load_dword v74, v37, s[12:13] offset:64
	s_mov_b64 exec, s[6:7]
	v_cmp_lt_i32_e32 vcc, v97, v108
	s_and_b64 exec, exec, vcc
	global_load_dword v85, v38, s[12:13]
	v_cmp_lt_i32_e32 vcc, v100, v108
	s_and_b64 exec, exec, vcc
	global_load_dword v84, v38, s[12:13] offset:32
	v_cmp_lt_i32_e32 vcc, v101, v108
	s_and_b64 exec, exec, vcc
	global_load_dword v109, v38, s[12:13] offset:64
	s_mov_b64 exec, s[6:7]
	v_cmp_lt_i32_e32 vcc, v97, v35
	s_and_b64 exec, exec, vcc
	global_load_dword v107, v39, s[12:13]
	v_cmp_lt_i32_e32 vcc, v100, v35
	s_and_b64 exec, exec, vcc
	global_load_dword v106, v39, s[12:13] offset:32
	v_cmp_lt_i32_e32 vcc, v101, v35
	s_and_b64 exec, exec, vcc
	global_load_dword v95, v39, s[12:13] offset:64
	s_mov_b64 exec, s[6:7]
	s_waitcnt lgkmcnt(0)
	s_barrier
	s_cmp_ge_i32 s36, s9
	s_cbranch_scc1 .LBB4_103
	s_cmp_lt_u32 s36, 8
	s_cbranch_scc1 .Lp1_noprio
	s_setprio 1

.LBB5_10:
	v_lshrrev_b32_e32 v2, 3, v0
	s_load_dwordx2 s[30:31], s[0:1], 0x40
	v_and_b32_e32 v1, 63, v0
	v_and_b32_e32 v2, 0x78, v2
	s_movk_i32 s2, 0xa0
	v_bfe_u32 v74, v0, 3, 3
	v_and_b32_e32 v75, 7, v0
	v_and_b32_e32 v77, 15, v0
	s_sub_i32 s0, s28, s20
	v_and_b32_e32 v5, 48, v0
	v_lshrrev_b32_e32 v0, 2, v0
	v_mad_u32_u24 v2, v2, s2, 0
	s_add_i32 s0, s0, 7
	v_mul_u32_u24_e32 v4, 0xa0, v75
	v_and_b32_e32 v0, 12, v0
	v_lshlrev_b32_e32 v76, 4, v75
	s_ashr_i32 s21, s0, 3
	v_cmp_eq_u32_e64 s[0:1], 0, v1
	v_mad_u32_u24 v3, v74, s2, v2
	v_add3_u32 v80, v2, v4, v5
	v_add_u32_e32 v2, 0, v5
	v_cmp_gt_u32_e64 s[4:5], 16, v1
	v_mul_u32_u24_e32 v1, 0x220, v77
	v_lshlrev_b32_e32 v32, 2, v0
	v_mbcnt_lo_u32_b32 v0, -1, 0
	v_mov_b32_e32 v33, 0
	v_or_b32_e32 v78, 8, v75
	v_or_b32_e32 v79, 16, v75
	v_lshlrev_b32_e32 v81, 3, v75
	v_cmp_gt_u32_e64 s[2:3], 8, v77
	s_mov_b32 s29, 0x3c800000
	v_add_u32_e32 v82, v3, v76
	v_add_u32_e32 v83, v2, v1
	v_add_u32_e32 v83, 0xcf10, v83
	v_mbcnt_hi_u32_b32 v84, -1, v0
	s_lshl_b32 s33, s38, 3
	s_add_i32 s33, s33, s20
	v_add_u32_e32 v8, s33, v74
	v_cmp_gt_i32_e32 vcc, s28, v8
	v_mov_b32_e32 v0, 0
	v_mov_b32_e32 v1, 0
	v_mov_b32_e32 v2, 0
	v_mov_b32_e32 v3, 0
	v_mov_b32_e32 v4, 0
	v_mov_b32_e32 v5, 0
	v_mov_b32_e32 v6, 0
	v_mov_b32_e32 v7, 0
	s_and_saveexec_b64 s[6:7], vcc
	v_lshl_add_u32 v9, v8, 1, v8
	v_lshlrev_b32_e32 v9, 2, v9
	global_load_dwordx4 v[4:7], v9, s[14:15]
	v_lshl_or_b32 v9, v8, 7, v76
	global_load_dwordx4 v[0:3], v9, s[12:13]
	s_mov_b64 exec, s[6:7]
	s_waitcnt vmcnt(3)
	ds_write_b128 v20, v[22:25]
	s_waitcnt vmcnt(2)
	ds_write_b128 v20, v[26:29] offset:17408
	s_and_saveexec_b64 s[6:7], s[40:41]
	ds_write_b128 v14, v[16:19] offset:52240
	s_mov_b64 exec, s[6:7]
	s_waitcnt vmcnt(1)
	v_sub_u32_e32 v58, v5, v4
	v_sub_u32_e32 v87, v6, v5
	v_sub_u32_e32 v85, v7, v6
	v_add_lshl_u32 v10, v4, v75, 2
	v_add_lshl_u32 v11, v5, v75, 2
	v_add_lshl_u32 v12, v6, v75, 2
	v_mov_b32_e32 v9, 0x186a0
	v_mov_b32_e32 v8, 0x186a0
	v_mov_b32_e32 v60, 0x186a0
	v_mov_b32_e32 v59, 0x186a0
	v_mov_b32_e32 v62, 0x186a0
	v_mov_b32_e32 v89, 0x186a0
	v_mov_b32_e32 v88, 0x186a0
	v_mov_b32_e32 v86, 0x186a0
	v_mov_b32_e32 v7, 0x186a0
	s_mov_b64 s[6:7], exec
	v_cmp_lt_i32_e32 vcc, v75, v58
	s_and_b64 exec, exec, vcc
	global_load_dword v9, v10, s[26:27]
	v_cmp_lt_i32_e32 vcc, v78, v58
	s_and_b64 exec, exec, vcc
	global_load_dword v8, v10, s[26:27] offset:32
	v_cmp_lt_i32_e32 vcc, v79, v58
	s_and_b64 exec, exec, vcc
	global_load_dword v60, v10, s[26:27] offset:64
	s_mov_b64 exec, s[6:7]
	v_cmp_lt_i32_e32 vcc, v75, v87
	s_and_b64 exec, exec, vcc
	global_load_dword v59, v11, s[26:27]
	v_cmp_lt_i32_e32 vcc, v78, v87
	s_and_b64 exec, exec, vcc
	global_load_dword v62, v11, s[26:27] offset:32
	v_cmp_lt_i32_e32 vcc, v79, v87
	s_and_b64 exec, exec, vcc
	global_load_dword v89, v11, s[26:27] offset:64
	s_mov_b64 exec, s[6:7]
	v_cmp_lt_i32_e32 vcc, v75, v85
	s_and_b64 exec, exec, vcc
	global_load_dword v88, v12, s[26:27]
	v_cmp_lt_i32_e32 vcc, v78, v85
	s_and_b64 exec, exec, vcc
	global_load_dword v86, v12, s[26:27] offset:32
	v_cmp_lt_i32_e32 vcc, v79, v85
	s_and_b64 exec, exec, vcc
	global_load_dword v7, v12, s[26:27] offset:64
	s_mov_b64 exec, s[6:7]
	s_waitcnt lgkmcnt(0)
	s_barrier
	s_cmp_ge_i32 s38, s21
	s_cbranch_scc1 .LBB5_118
	s_cmp_lt_u32 s38, 8
	s_cbranch_scc1 .Lp2_noprio
	s_setprio 1
